# s22 + P0 does no MoE conversion items: its 6848 items (140 MB) join P4's slice, converted by the gating / converter workgroups while the scan still runs (P0 is bandwidth-bound)
# baseline (speedup 1.0000x reference)
; #define MOE_RANGE(first_, end_, stride_) do { f32x4 rgA_[16], rgB_[16]; int ia_ = (first_); if (ia_ < (end_)) MOE_LOAD(ia_, rgA_); \
;         while (ia_ < (end_)) { const int ib_ = ia_ + (stride_); if (ib_ < (end_)) MOE_LOAD(ib_, rgB_); MOE_FIN(ia_, rgA_); if (ib_ >= (end_)) break; \
;             ia_ = ib_ + (stride_); if (ia_ < (end_)) MOE_LOAD(ia_, rgA_); MOE_FIN(ib_, rgB_); } } while (0)
; __global__ void __launch_bounds__(NTHREADS, 2) fwd(Args args) {
;     ...
;             MOE_RANGE(gw, CV_P0 - CVBG - CVSK, NGW);
.LBB0_70:
	s_cmpk_lt_i32 s50, 0
	s_cbranch_scc0 .LBB0_72
	s_ashr_i32 s0, s50, 31
	s_lshr_b32 s0, s0, 21
	s_add_i32 s1, s50, s0
	s_ashr_i32 s0, s1, 11
	s_and_b32 s1, s1, 0xf800
	s_sub_i32 s3, s50, s1
	s_ashr_i32 s1, s0, 31
	s_lshl_b64 s[0:1], s[0:1], 25
	s_add_u32 s4, s66, s0
	s_sext_i32_i16 s0, s3
	s_addc_u32 s5, s67, s1
	s_bfe_u32 s0, s0, 0x70018
	s_add_i32 s0, s3, s0
	s_sext_i32_i16 s1, s0
	s_and_b32 s0, s0, 0xff80
	s_sub_i32 s0, s3, s0
	s_sext_i32_i16 s0, s0
	s_and_b32 s1, s1, 0xffffff80
	s_lshl_b32 s0, s0, 5
	v_or_b32_e32 v50, s1, v1
	s_ashr_i32 s1, s0, 31
	s_lshl_b64 s[0:1], s[0:1], 2
	s_add_u32 s0, s4, s0
	s_waitcnt vmcnt(10)
	v_or_b32_e32 v4, 8, v50
	s_waitcnt vmcnt(8)
	v_or_b32_e32 v10, 16, v50
	v_or_b32_e32 v12, 24, v50
	s_waitcnt vmcnt(6)
	v_or_b32_e32 v18, 32, v50
	v_or_b32_e32 v20, 40, v50
	s_waitcnt vmcnt(4)
	v_or_b32_e32 v26, 48, v50
	v_or_b32_e32 v28, 56, v50
	v_or_b32_e32 v34, 64, v50
	v_or_b32_e32 v36, 0x48, v50
	v_or_b32_e32 v42, 0x50, v50
	v_or_b32_e32 v44, 0x58, v50
	v_or_b32_e32 v54, 0x60, v50
	s_addc_u32 s1, s5, s1
	v_mov_b32_e32 v131, 0
	v_ashrrev_i32_e32 v51, 31, v50
	v_ashrrev_i32_e32 v5, 31, v4
	v_ashrrev_i32_e32 v11, 31, v10
	v_ashrrev_i32_e32 v13, 31, v12
	v_ashrrev_i32_e32 v19, 31, v18
	v_ashrrev_i32_e32 v21, 31, v20
	v_ashrrev_i32_e32 v27, 31, v26
	v_ashrrev_i32_e32 v29, 31, v28
	v_ashrrev_i32_e32 v35, 31, v34
	v_ashrrev_i32_e32 v37, 31, v36
	v_ashrrev_i32_e32 v43, 31, v42
	v_ashrrev_i32_e32 v45, 31, v44
	v_ashrrev_i32_e32 v55, 31, v54
	v_or_b32_e32 v56, 0x68, v50
	v_lshl_add_u64 v[52:53], s[0:1], 0, v[130:131]
	v_lshlrev_b64 v[2:3], 14, v[50:51]
	v_lshlrev_b64 v[4:5], 14, v[4:5]
	v_lshlrev_b64 v[10:11], 14, v[10:11]
	v_lshlrev_b64 v[12:13], 14, v[12:13]
	v_lshlrev_b64 v[18:19], 14, v[18:19]
	v_lshlrev_b64 v[20:21], 14, v[20:21]
	v_lshlrev_b64 v[26:27], 14, v[26:27]
	v_lshlrev_b64 v[28:29], 14, v[28:29]
	v_lshlrev_b64 v[34:35], 14, v[34:35]
	v_lshlrev_b64 v[36:37], 14, v[36:37]
	v_lshlrev_b64 v[42:43], 14, v[42:43]
	v_lshlrev_b64 v[44:45], 14, v[44:45]
	v_lshlrev_b64 v[54:55], 14, v[54:55]
	v_ashrrev_i32_e32 v57, 31, v56
	v_lshl_add_u64 v[2:3], v[52:53], 0, v[2:3]
	v_lshl_add_u64 v[6:7], v[52:53], 0, v[4:5]
	v_lshl_add_u64 v[10:11], v[52:53], 0, v[10:11]
	v_lshl_add_u64 v[14:15], v[52:53], 0, v[12:13]
	v_lshl_add_u64 v[18:19], v[52:53], 0, v[18:19]
	v_lshl_add_u64 v[22:23], v[52:53], 0, v[20:21]
	v_lshl_add_u64 v[26:27], v[52:53], 0, v[26:27]
	v_lshl_add_u64 v[30:31], v[52:53], 0, v[28:29]
	v_lshl_add_u64 v[34:35], v[52:53], 0, v[34:35]
	v_lshl_add_u64 v[38:39], v[52:53], 0, v[36:37]
	v_lshl_add_u64 v[42:43], v[52:53], 0, v[42:43]
	v_lshl_add_u64 v[46:47], v[52:53], 0, v[44:45]
	v_lshl_add_u64 v[54:55], v[52:53], 0, v[54:55]
	v_lshlrev_b64 v[56:57], 14, v[56:57]
	global_load_dwordx4 v[2:5], v[2:3], off nt
	s_nop 0
	global_load_dwordx4 v[6:9], v[6:7], off nt
	s_nop 0
	global_load_dwordx4 v[10:13], v[10:11], off nt
	s_nop 0
	global_load_dwordx4 v[14:17], v[14:15], off nt
	s_nop 0
	global_load_dwordx4 v[18:21], v[18:19], off nt
	s_nop 0
	global_load_dwordx4 v[22:25], v[22:23], off nt
	s_nop 0
	global_load_dwordx4 v[26:29], v[26:27], off nt
	s_nop 0
	global_load_dwordx4 v[30:33], v[30:31], off nt
	s_nop 0
	global_load_dwordx4 v[34:37], v[34:35], off nt
	s_nop 0
	global_load_dwordx4 v[38:41], v[38:39], off nt
	s_nop 0
	global_load_dwordx4 v[42:45], v[42:43], off nt
	s_nop 0
	global_load_dwordx4 v[46:49], v[46:47], off nt
	v_lshl_add_u64 v[56:57], v[52:53], 0, v[56:57]
	global_load_dwordx4 v[66:69], v[54:55], off nt
	global_load_dwordx4 v[70:73], v[56:57], off nt
	v_or_b32_e32 v54, 0x70, v50
	v_ashrrev_i32_e32 v55, 31, v54
	v_or_b32_e32 v50, 0x78, v50
	v_lshlrev_b64 v[54:55], 14, v[54:55]
	v_ashrrev_i32_e32 v51, 31, v50
	v_lshl_add_u64 v[54:55], v[52:53], 0, v[54:55]
	v_lshlrev_b64 v[50:51], 14, v[50:51]
	v_lshl_add_u64 v[50:51], v[52:53], 0, v[50:51]
	global_load_dwordx4 v[90:93], v[54:55], off nt
	global_load_dwordx4 v[94:97], v[50:51], off nt

.LBB0_75:
	s_cmpk_gt_i32 s2, -1
	s_mov_b64 s[0:1], -1
	s_cbranch_scc1 .LBB0_74
	s_add_i32 s3, s2, s92
	s_cmpk_lt_i32 s3, 0
	s_cselect_b64 s[4:5], -1, 0
	s_cmpk_gt_i32 s3, -1
	s_cselect_b64 s[0:1], -1, 0
	s_and_b64 vcc, exec, s[0:1]
	s_cbranch_vccnz .LBB0_78
	s_ashr_i32 s6, s3, 31
	s_lshr_b32 s6, s6, 21
	s_add_i32 s6, s3, s6
	s_and_b32 s7, s6, 0xf800
	s_ashr_i32 s6, s6, 11
	s_sub_i32 s8, s3, s7
	s_ashr_i32 s7, s6, 31
	s_lshl_b64 s[6:7], s[6:7], 25
	s_add_u32 s9, s66, s6
	s_sext_i32_i16 s6, s8
	s_addc_u32 s10, s67, s7
	s_bfe_u32 s6, s6, 0x70018
	s_add_i32 s6, s8, s6
	s_sext_i32_i16 s7, s6
	s_and_b32 s6, s6, 0xff80
	s_sub_i32 s6, s8, s6
	s_sext_i32_i16 s6, s6
	s_and_b32 s7, s7, 0xffffff80
	s_lshl_b32 s6, s6, 5
	v_or_b32_e32 v122, s7, v1
	s_ashr_i32 s7, s6, 31
	s_lshl_b64 s[6:7], s[6:7], 2
	v_ashrrev_i32_e32 v123, 31, v122
	s_add_u32 s6, s9, s6
	v_lshlrev_b64 v[50:51], 14, v[122:123]
	v_or_b32_e32 v52, 8, v122
	v_or_b32_e32 v58, 16, v122
	v_or_b32_e32 v60, 24, v122
	v_or_b32_e32 v74, 32, v122
	v_or_b32_e32 v76, 40, v122
	v_or_b32_e32 v82, 48, v122
	v_or_b32_e32 v84, 56, v122
	v_or_b32_e32 v98, 64, v122
	v_or_b32_e32 v100, 0x48, v122
	v_or_b32_e32 v106, 0x50, v122
	v_or_b32_e32 v108, 0x58, v122
	v_or_b32_e32 v114, 0x60, v122
	v_or_b32_e32 v116, 0x68, v122
	v_or_b32_e32 v126, 0x70, v122
	v_or_b32_e32 v122, 0x78, v122
	s_addc_u32 s7, s10, s7
	v_ashrrev_i32_e32 v53, 31, v52
	v_ashrrev_i32_e32 v59, 31, v58
	v_ashrrev_i32_e32 v61, 31, v60
	v_ashrrev_i32_e32 v75, 31, v74
	v_ashrrev_i32_e32 v77, 31, v76
	v_ashrrev_i32_e32 v83, 31, v82
	v_ashrrev_i32_e32 v85, 31, v84
	v_ashrrev_i32_e32 v99, 31, v98
	v_ashrrev_i32_e32 v101, 31, v100
	v_ashrrev_i32_e32 v107, 31, v106
	v_ashrrev_i32_e32 v109, 31, v108
	v_ashrrev_i32_e32 v115, 31, v114
	v_ashrrev_i32_e32 v117, 31, v116
	v_ashrrev_i32_e32 v127, 31, v126
	v_ashrrev_i32_e32 v123, 31, v122
	v_lshl_add_u64 v[124:125], s[6:7], 0, v[130:131]
	v_lshlrev_b64 v[52:53], 14, v[52:53]
	v_lshlrev_b64 v[58:59], 14, v[58:59]
	v_lshlrev_b64 v[60:61], 14, v[60:61]
	v_lshlrev_b64 v[74:75], 14, v[74:75]
	v_lshlrev_b64 v[76:77], 14, v[76:77]
	v_lshlrev_b64 v[82:83], 14, v[82:83]
	v_lshlrev_b64 v[84:85], 14, v[84:85]
	v_lshlrev_b64 v[98:99], 14, v[98:99]
	v_lshlrev_b64 v[100:101], 14, v[100:101]
	v_lshlrev_b64 v[106:107], 14, v[106:107]
	v_lshlrev_b64 v[108:109], 14, v[108:109]
	v_lshlrev_b64 v[114:115], 14, v[114:115]
	v_lshlrev_b64 v[116:117], 14, v[116:117]
	v_lshlrev_b64 v[126:127], 14, v[126:127]
	v_lshlrev_b64 v[122:123], 14, v[122:123]
	v_lshl_add_u64 v[50:51], v[124:125], 0, v[50:51]
	v_lshl_add_u64 v[54:55], v[124:125], 0, v[52:53]
	v_lshl_add_u64 v[58:59], v[124:125], 0, v[58:59]
	v_lshl_add_u64 v[62:63], v[124:125], 0, v[60:61]
	v_lshl_add_u64 v[74:75], v[124:125], 0, v[74:75]
	v_lshl_add_u64 v[78:79], v[124:125], 0, v[76:77]
	v_lshl_add_u64 v[82:83], v[124:125], 0, v[82:83]
	v_lshl_add_u64 v[86:87], v[124:125], 0, v[84:85]
	v_lshl_add_u64 v[98:99], v[124:125], 0, v[98:99]
	v_lshl_add_u64 v[102:103], v[124:125], 0, v[100:101]
	v_lshl_add_u64 v[106:107], v[124:125], 0, v[106:107]
	v_lshl_add_u64 v[110:111], v[124:125], 0, v[108:109]
	v_lshl_add_u64 v[114:115], v[124:125], 0, v[114:115]
	v_lshl_add_u64 v[118:119], v[124:125], 0, v[116:117]
	v_lshl_add_u64 v[126:127], v[124:125], 0, v[126:127]
	v_lshl_add_u64 v[128:129], v[124:125], 0, v[122:123]
	global_load_dwordx4 v[50:53], v[50:51], off nt
	s_nop 0
	global_load_dwordx4 v[54:57], v[54:55], off nt
	s_nop 0
	global_load_dwordx4 v[58:61], v[58:59], off nt
	s_nop 0
	global_load_dwordx4 v[62:65], v[62:63], off nt
	s_nop 0
	global_load_dwordx4 v[74:77], v[74:75], off nt
	s_nop 0
	global_load_dwordx4 v[78:81], v[78:79], off nt
	s_nop 0
	global_load_dwordx4 v[82:85], v[82:83], off nt
	s_nop 0
	global_load_dwordx4 v[86:89], v[86:87], off nt
	s_nop 0
	global_load_dwordx4 v[98:101], v[98:99], off nt
	s_nop 0
	global_load_dwordx4 v[102:105], v[102:103], off nt
	s_nop 0
	global_load_dwordx4 v[106:109], v[106:107], off nt
	s_nop 0
	global_load_dwordx4 v[110:113], v[110:111], off nt
	s_nop 0
	global_load_dwordx4 v[114:117], v[114:115], off nt
	s_nop 0
	global_load_dwordx4 v[118:121], v[118:119], off nt
	s_nop 0
	global_load_dwordx4 v[122:125], v[126:127], off nt
	s_nop 0
	global_load_dwordx4 v[126:129], v[128:129], off nt
; #define LAS __attribute__((address_space(3)))
; #define LDS_WAIT() asm volatile("s_waitcnt lgkmcnt(0)" ::: "memory")
; __device__ __forceinline__ void item8_finish(int K, unsigned char* WT, int k0, int r0, LAS float* scr, int lane, const f32x4 (&rg)[16]) {
; #pragma unroll
;     for (int i = 0; i < 16; ++i) { LAS float* d = scr + (8 * i + (lane >> 3)) * 33 + 4 * (lane & 7); d[0] = rg[i].x; d[1] = rg[i].y; d[2] = rg[i].z; d[3] = rg[i].w; }
;     LDS_WAIT();
;     const int c = lane & 7;
; #pragma unroll
;     for (int j = 0; j < 4; ++j) { const int n = (lane >> 3) + 8 * j; const LAS float* sp = scr + (16 * c) * 33 + n; int w[4];
; #pragma unroll
;         for (int q = 0; q < 4; ++q) { w[q] = __builtin_amdgcn_cvt_pk_fp8_f32(sp[(4 * q) * 33] * 256.f, sp[(4 * q + 1) * 33] * 256.f, 0, false); w[q] = __builtin_amdgcn_cvt_pk_fp8_f32(sp[(4 * q + 2) * 33] * 256.f, sp[(4 * q + 3) * 33] * 256.f, w[q], true); }
.LBB0_78:
	s_ashr_i32 s6, s2, 31
	s_lshr_b32 s6, s6, 21
	s_add_i32 s7, s2, s6
	v_add_u32_e32 v142, v138, v139
	s_ashr_i32 s6, s7, 11
	s_and_b32 s7, s7, 0xf800
	v_add_u32_e32 v143, 0x420, v142
	v_add_u32_e32 v144, 0x428, v142
	v_add_u32_e32 v145, 0x840, v142
	v_add_u32_e32 v146, 0x848, v142
	v_add_u32_e32 v147, 0xc60, v142
	v_add_u32_e32 v148, 0xc68, v142
	v_add_u32_e32 v149, 0x1080, v142
	v_add_u32_e32 v150, 0x1088, v142
	v_add_u32_e32 v151, 0x14a0, v142
	v_add_u32_e32 v152, 0x14a8, v142
	v_add_u32_e32 v153, 0x18c0, v142
	v_add_u32_e32 v154, 0x18c8, v142
	v_add_u32_e32 v155, 0x1ce0, v142
	v_add_u32_e32 v156, 0x1ce8, v142
	v_add_u32_e32 v157, 0x2100, v142
	v_add_u32_e32 v158, 0x2108, v142
	v_add_u32_e32 v159, 0x2520, v142
	v_add_u32_e32 v160, 0x2528, v142
	v_add_u32_e32 v161, 0x2940, v142
	v_add_u32_e32 v162, 0x2948, v142
	v_add_u32_e32 v163, 0x2d60, v142
	v_add_u32_e32 v164, 0x2d68, v142
	v_add_u32_e32 v165, 0x3180, v142
	v_add_u32_e32 v166, 0x3188, v142
	v_add_u32_e32 v167, 0x35a0, v142
	v_add_u32_e32 v168, 0x35a8, v142
	v_add_u32_e32 v169, 0x39c0, v142
	v_add_u32_e32 v170, 0x39c8, v142
	v_add_u32_e32 v171, 0x3de0, v142
	v_add_u32_e32 v172, 0x3de8, v142
	s_sub_i32 s7, s2, s7
	s_waitcnt vmcnt(10)
	ds_write2_b32 v142, v2, v3 offset1:1
	ds_write2_b32 v142, v4, v5 offset0:2 offset1:3
	ds_write2_b32 v143, v6, v7 offset1:1
	ds_write2_b32 v144, v8, v9 offset1:1
	s_waitcnt vmcnt(8)
	ds_write2_b32 v145, v10, v11 offset1:1
	ds_write2_b32 v146, v12, v13 offset1:1
	ds_write2_b32 v147, v14, v15 offset1:1
	ds_write2_b32 v148, v16, v17 offset1:1
	s_waitcnt vmcnt(6)
	ds_write2_b32 v149, v18, v19 offset1:1
	ds_write2_b32 v150, v20, v21 offset1:1
	ds_write2_b32 v151, v22, v23 offset1:1
	ds_write2_b32 v152, v24, v25 offset1:1
	s_waitcnt vmcnt(4)
	ds_write2_b32 v153, v26, v27 offset1:1
	ds_write2_b32 v154, v28, v29 offset1:1
	ds_write2_b32 v155, v30, v31 offset1:1
	ds_write2_b32 v156, v32, v33 offset1:1
	ds_write2_b32 v157, v34, v35 offset1:1
	ds_write2_b32 v158, v36, v37 offset1:1
	ds_write2_b32 v159, v38, v39 offset1:1
	ds_write2_b32 v160, v40, v41 offset1:1
	ds_write2_b32 v161, v42, v43 offset1:1
	ds_write2_b32 v162, v44, v45 offset1:1
	ds_write2_b32 v163, v46, v47 offset1:1
	ds_write2_b32 v164, v48, v49 offset1:1
	s_waitcnt vmcnt(3)
	ds_write2_b32 v165, v66, v67 offset1:1
	ds_write2_b32 v166, v68, v69 offset1:1
	s_waitcnt vmcnt(2)
	ds_write2_b32 v167, v70, v71 offset1:1
	ds_write2_b32 v168, v72, v73 offset1:1
	s_waitcnt vmcnt(1)
	ds_write2_b32 v169, v90, v91 offset1:1
	ds_write2_b32 v170, v92, v93 offset1:1
	s_waitcnt vmcnt(0)
	ds_write2_b32 v171, v94, v95 offset1:1
	ds_write2_b32 v172, v96, v97 offset1:1
	s_sext_i32_i16 s8, s7
	s_waitcnt lgkmcnt(0)
	s_bfe_u32 s8, s8, 0x70018
	ds_read2_b32 v[178:179], v140 offset1:8
	ds_read2_b32 v[180:181], v140 offset0:33 offset1:41
	s_add_i32 s8, s7, s8
	s_sext_i32_i16 s9, s8
	s_and_b32 s8, s8, 0xff80
	s_sub_i32 s7, s7, s8
	s_bfe_i32 s10, s7, 0x80000
	ds_read2_b32 v[184:185], v140 offset0:66 offset1:74
	ds_read2_b32 v[186:187], v140 offset0:99 offset1:107
	s_bfe_u32 s10, s10, 0x60009
	s_waitcnt lgkmcnt(3)
	v_mul_f32_e32 v141, 0x43800000, v178
	s_waitcnt lgkmcnt(2)
	v_mul_f32_e32 v173, 0x43800000, v180
	v_mov_b32_e32 v174, 0
	ds_read2_b32 v[188:189], v140 offset0:132 offset1:140
	ds_read2_b32 v[190:191], v140 offset0:165 offset1:173
	s_lshl_b32 s8, s7, 5
	s_add_i32 s7, s7, s10
	v_cvt_pk_fp8_f32 v174, v141, v173
	s_bfe_i32 s7, s7, 0x80000
	s_sext_i32_i16 s10, s7
	s_sext_i32_i16 s7, s8
	s_bfe_u32 s7, s7, 0xb0014
	s_waitcnt lgkmcnt(3)
	v_mul_f32_e32 v141, 0x43800000, v184
	s_waitcnt lgkmcnt(2)
	v_mul_f32_e32 v173, 0x43800000, v186
	s_add_i32 s7, s8, s7
	v_cvt_pk_fp8_f32 v174, v141, v173 op_sel:[0,0,1]
	s_waitcnt lgkmcnt(1)
	v_mul_f32_e32 v141, 0x43800000, v188
	s_waitcnt lgkmcnt(0)
	v_mul_f32_e32 v173, 0x43800000, v190
	v_mov_b32_e32 v175, 0
	s_and_b32 s7, s7, 0xf800
	v_cvt_pk_fp8_f32 v175, v141, v173
	ds_read2_b32 v[192:193], v140 offset0:198 offset1:206
	ds_read2_b32 v[196:197], v140 offset0:231 offset1:239
	v_add_u32_e32 v141, 0x400, v140
	s_sub_i32 s8, s8, s7
	s_ashr_i32 s7, s6, 31
	ds_read2_b32 v[198:199], v141 offset0:8 offset1:16
	ds_read2_b32 v[200:201], v141 offset0:41 offset1:49
	s_lshl_b64 s[6:7], s[6:7], 23
	ds_read2_b32 v[202:203], v141 offset0:74 offset1:82
	ds_read2_b32 v[204:205], v141 offset0:107 offset1:115
	ds_read2_b32 v[206:207], v141 offset0:140 offset1:148
	ds_read2_b32 v[208:209], v141 offset0:173 offset1:181
	s_add_u32 s11, s93, s6
	v_readlane_b32 s6, v246, 22
	s_addc_u32 s7, s6, s7
	s_sext_i32_i16 s6, s8
	s_bfe_u32 s6, s6, 0x70018
	s_waitcnt lgkmcnt(7)
	v_mul_f32_e32 v173, 0x43800000, v192
	s_waitcnt lgkmcnt(6)
	v_mul_f32_e32 v176, 0x43800000, v196
	s_add_i32 s6, s8, s6
	v_cvt_pk_fp8_f32 v175, v173, v176 op_sel:[0,0,1]
	s_waitcnt lgkmcnt(5)
	v_mul_f32_e32 v173, 0x43800000, v198
	s_waitcnt lgkmcnt(4)
	v_mul_f32_e32 v177, 0x43800000, v200
	v_mov_b32_e32 v176, 0
	ds_read2_b32 v[210:211], v141 offset0:206 offset1:214
	ds_read2_b32 v[212:213], v141 offset0:239 offset1:247
	s_sext_i32_i16 s12, s6
	s_and_b32 s6, s6, 0xff80
	v_cvt_pk_fp8_f32 v176, v173, v177
	s_waitcnt lgkmcnt(3)
	v_mul_f32_e32 v180, 0x43800000, v206
	s_waitcnt lgkmcnt(2)
	v_mul_f32_e32 v184, 0x43800000, v208
	v_mov_b32_e32 v177, 0
	s_lshl_b32 s10, s10, 1
	s_sub_i32 s6, s8, s6
	v_cvt_pk_fp8_f32 v177, v180, v184
	s_lshl_b32 s12, s12, 1
	s_and_b32 s10, s10, 0xffffff80
	s_sext_i32_i16 s6, s6
	s_and_b32 s9, s9, 0xffffff80
	s_and_b32 s12, s12, 0xffffff00
	s_add_i32 s6, s10, s6
	v_mul_f32_e32 v173, 0x43800000, v202
	v_mul_f32_e32 v178, 0x43800000, v204
	s_add_i32 s6, s6, s12
	s_ashr_i32 s10, s9, 31
	v_cvt_pk_fp8_f32 v176, v173, v178 op_sel:[0,0,1]
	s_waitcnt lgkmcnt(1)
; #define LAS __attribute__((address_space(3)))
; #define LDS_WAIT() asm volatile("s_waitcnt lgkmcnt(0)" ::: "memory")
; __device__ __forceinline__ void item8_finish(int K, unsigned char* WT, int k0, int r0, LAS float* scr, int lane, const f32x4 (&rg)[16]) {
; #pragma unroll
;     for (int i = 0; i < 16; ++i) { LAS float* d = scr + (8 * i + (lane >> 3)) * 33 + 4 * (lane & 7); d[0] = rg[i].x; d[1] = rg[i].y; d[2] = rg[i].z; d[3] = rg[i].w; }
;     LDS_WAIT();
;     const int c = lane & 7;
; #pragma unroll
;     for (int j = 0; j < 4; ++j) { const int n = (lane >> 3) + 8 * j; const LAS float* sp = scr + (16 * c) * 33 + n; int w[4];
; #pragma unroll
;         for (int q = 0; q < 4; ++q) { w[q] = __builtin_amdgcn_cvt_pk_fp8_f32(sp[(4 * q) * 33] * 256.f, sp[(4 * q + 1) * 33] * 256.f, 0, false); w[q] = __builtin_amdgcn_cvt_pk_fp8_f32(sp[(4 * q + 2) * 33] * 256.f, sp[(4 * q + 3) * 33] * 256.f, w[q], true); }
;         u32x4 o; o.x = (unsigned)w[0]; o.y = (unsigned)w[1]; o.z = (unsigned)w[2]; o.w = (unsigned)w[3];
;         __builtin_nontemporal_store(o, (u32x4*)(WT + (size_t)(r0 + n) * K + k0 + 16 * c)); }
;     LDS_WAIT();
; }
	v_mul_f32_e32 v173, 0x43800000, v210
	s_waitcnt lgkmcnt(0)
	v_mul_f32_e32 v178, 0x43800000, v212
	s_add_u32 s8, s11, s9
	v_cvt_pk_fp8_f32 v177, v173, v178 op_sel:[0,0,1]
	v_or_b32_e32 v214, s6, v1
	s_addc_u32 s9, s7, s10
	v_ashrrev_i32_e32 v215, 31, v214
	v_lshl_add_u64 v[182:183], s[8:9], 0, v[132:133]
	v_lshlrev_b64 v[214:215], 11, v[214:215]
	v_lshl_add_u64 v[214:215], v[182:183], 0, v[214:215]
	global_store_dwordx4 v[214:215], v[174:177], off nt
	v_mul_f32_e32 v173, 0x43800000, v179
	v_mul_f32_e32 v178, 0x43800000, v191
	v_mul_f32_e32 v175, 0x43800000, v181
	v_mov_b32_e32 v174, 0
	v_cvt_pk_fp8_f32 v174, v173, v175
	v_mul_f32_e32 v177, 0x43800000, v189
	v_mov_b32_e32 v175, 0
	v_cvt_pk_fp8_f32 v175, v177, v178
	v_mul_f32_e32 v173, 0x43800000, v185
	v_mul_f32_e32 v176, 0x43800000, v187
	v_cvt_pk_fp8_f32 v174, v173, v176 op_sel:[0,0,1]
	v_mul_f32_e32 v173, 0x43800000, v193
	v_mul_f32_e32 v176, 0x43800000, v197
	v_cvt_pk_fp8_f32 v175, v173, v176 op_sel:[0,0,1]
	v_mul_f32_e32 v173, 0x43800000, v199
	v_mul_f32_e32 v177, 0x43800000, v201
	v_mov_b32_e32 v176, 0
	v_cvt_pk_fp8_f32 v176, v173, v177
	v_mul_f32_e32 v179, 0x43800000, v207
	v_mul_f32_e32 v180, 0x43800000, v209
	v_mov_b32_e32 v177, 0
	v_cvt_pk_fp8_f32 v177, v179, v180
	v_mul_f32_e32 v173, 0x43800000, v203
	v_mul_f32_e32 v178, 0x43800000, v205
	v_cvt_pk_fp8_f32 v176, v173, v178 op_sel:[0,0,1]
	v_mul_f32_e32 v173, 0x43800000, v211
	v_mul_f32_e32 v178, 0x43800000, v213
	v_cvt_pk_fp8_f32 v177, v173, v178 op_sel:[0,0,1]
	v_or_b32_e32 v178, s6, v135
	v_ashrrev_i32_e32 v179, 31, v178
	ds_read2_b32 v[180:181], v140 offset0:16 offset1:24
	ds_read2_b32 v[184:185], v140 offset0:49 offset1:57
	v_lshlrev_b64 v[178:179], 11, v[178:179]
	v_lshl_add_u64 v[178:179], v[182:183], 0, v[178:179]
	global_store_dwordx4 v[178:179], v[174:177], off nt
	ds_read2_b32 v[178:179], v140 offset0:82 offset1:90
	ds_read2_b32 v[186:187], v140 offset0:115 offset1:123
	s_waitcnt lgkmcnt(3)
	v_mul_f32_e32 v173, 0x43800000, v180
	s_waitcnt lgkmcnt(2)
	v_mul_f32_e32 v175, 0x43800000, v184
	v_mov_b32_e32 v174, 0
	ds_read2_b32 v[188:189], v140 offset0:148 offset1:156
	ds_read2_b32 v[190:191], v140 offset0:181 offset1:189
	v_cvt_pk_fp8_f32 v174, v173, v175
	s_waitcnt lgkmcnt(3)
	v_mul_f32_e32 v173, 0x43800000, v178
	s_waitcnt lgkmcnt(2)
	v_mul_f32_e32 v175, 0x43800000, v186
	ds_read2_b32 v[192:193], v140 offset0:214 offset1:222
	ds_read2_b32 v[196:197], v140 offset0:247 offset1:255
	v_cvt_pk_fp8_f32 v174, v173, v175 op_sel:[0,0,1]
	s_waitcnt lgkmcnt(3)
	v_mul_f32_e32 v173, 0x43800000, v188
	s_waitcnt lgkmcnt(2)
	v_mul_f32_e32 v176, 0x43800000, v190
	v_mov_b32_e32 v175, 0
	ds_read2_b32 v[198:199], v141 offset0:24 offset1:32
	ds_read2_b32 v[200:201], v141 offset0:57 offset1:65
	v_cvt_pk_fp8_f32 v175, v173, v176
	ds_read2_b32 v[202:203], v141 offset0:90 offset1:98
	ds_read2_b32 v[204:205], v141 offset0:123 offset1:131
	ds_read2_b32 v[206:207], v141 offset0:156 offset1:164
	ds_read2_b32 v[208:209], v141 offset0:189 offset1:197
	s_waitcnt lgkmcnt(7)
	v_mul_f32_e32 v173, 0x43800000, v192
	s_waitcnt lgkmcnt(6)
	v_mul_f32_e32 v176, 0x43800000, v196
	v_cvt_pk_fp8_f32 v175, v173, v176 op_sel:[0,0,1]
	s_waitcnt lgkmcnt(5)
	v_mul_f32_e32 v173, 0x43800000, v198
	s_waitcnt lgkmcnt(4)
	v_mul_f32_e32 v177, 0x43800000, v200
	v_mov_b32_e32 v176, 0
	v_cvt_pk_fp8_f32 v176, v173, v177
	v_add_u32_e32 v173, 0x600, v140
	ds_read2_b32 v[210:211], v141 offset0:222 offset1:230
	ds_read2_b32 v[212:213], v173 offset0:127 offset1:135
	s_waitcnt lgkmcnt(3)
	v_mul_f32_e32 v184, 0x43800000, v206
	s_waitcnt lgkmcnt(2)
	v_mul_f32_e32 v186, 0x43800000, v208
	v_mov_b32_e32 v177, 0
	v_cvt_pk_fp8_f32 v177, v184, v186
	v_mul_f32_e32 v178, 0x43800000, v202
	v_mul_f32_e32 v180, 0x43800000, v204
	v_cvt_pk_fp8_f32 v176, v178, v180 op_sel:[0,0,1]
	s_waitcnt lgkmcnt(1)
	v_mul_f32_e32 v178, 0x43800000, v210
	s_waitcnt lgkmcnt(0)
	v_mul_f32_e32 v180, 0x43800000, v212
	v_cvt_pk_fp8_f32 v177, v178, v180 op_sel:[0,0,1]
	v_or_b32_e32 v214, s6, v136
	v_ashrrev_i32_e32 v215, 31, v214
	v_lshlrev_b64 v[214:215], 11, v[214:215]
	v_lshl_add_u64 v[214:215], v[182:183], 0, v[214:215]
	global_store_dwordx4 v[214:215], v[174:177], off nt
	v_mul_f32_e32 v178, 0x43800000, v189
	v_mul_f32_e32 v180, 0x43800000, v207
	v_mul_f32_e32 v175, 0x43800000, v181
	v_mul_f32_e32 v176, 0x43800000, v185
	v_mov_b32_e32 v174, 0
	v_cvt_pk_fp8_f32 v174, v175, v176
	v_mul_f32_e32 v176, 0x43800000, v179
	v_mul_f32_e32 v179, 0x43800000, v191
	v_mov_b32_e32 v175, 0
	v_cvt_pk_fp8_f32 v175, v178, v179
	v_mul_f32_e32 v177, 0x43800000, v187
	v_cvt_pk_fp8_f32 v174, v176, v177 op_sel:[0,0,1]
	v_mul_f32_e32 v176, 0x43800000, v193
	v_mul_f32_e32 v177, 0x43800000, v197
	v_cvt_pk_fp8_f32 v175, v176, v177 op_sel:[0,0,1]
	v_mul_f32_e32 v177, 0x43800000, v199
	v_mul_f32_e32 v178, 0x43800000, v201
	v_mov_b32_e32 v176, 0
	v_cvt_pk_fp8_f32 v176, v177, v178
	v_mul_f32_e32 v181, 0x43800000, v209
	v_mov_b32_e32 v177, 0
	v_cvt_pk_fp8_f32 v177, v180, v181
	v_mul_f32_e32 v178, 0x43800000, v203
	v_mul_f32_e32 v179, 0x43800000, v205
	v_cvt_pk_fp8_f32 v176, v178, v179 op_sel:[0,0,1]
	v_mul_f32_e32 v178, 0x43800000, v211
	v_mul_f32_e32 v179, 0x43800000, v213
	v_cvt_pk_fp8_f32 v177, v178, v179 op_sel:[0,0,1]
	v_or_b32_e32 v178, s6, v137
	v_ashrrev_i32_e32 v179, 31, v178
	v_lshlrev_b64 v[178:179], 11, v[178:179]
	v_lshl_add_u64 v[178:179], v[182:183], 0, v[178:179]
	global_store_dwordx4 v[178:179], v[174:177], off nt
	s_waitcnt lgkmcnt(0)
	s_andn2_b64 vcc, exec, s[4:5]
	s_cbranch_vccnz .LBB0_74
	s_add_i32 s2, s3, s92
	s_cmpk_gt_i32 s2, -1
	s_cbranch_scc1 .LBB0_73
	s_ashr_i32 s4, s2, 31
	s_lshr_b32 s4, s4, 21
	s_add_i32 s5, s2, s4
	s_ashr_i32 s4, s5, 11
	s_and_b32 s5, s5, 0xf800
	s_sub_i32 s6, s2, s5
	s_ashr_i32 s5, s4, 31
	s_lshl_b64 s[4:5], s[4:5], 25
	s_add_u32 s7, s66, s4
	s_sext_i32_i16 s4, s6
	s_addc_u32 s8, s67, s5
	s_bfe_u32 s4, s4, 0x70018
	s_add_i32 s4, s6, s4
	s_sext_i32_i16 s5, s4
	s_and_b32 s4, s4, 0xff80
	s_sub_i32 s4, s6, s4
	s_sext_i32_i16 s4, s4
	s_and_b32 s5, s5, 0xffffff80
	s_lshl_b32 s4, s4, 5
	v_or_b32_e32 v90, s5, v1
	s_ashr_i32 s5, s4, 31
	s_lshl_b64 s[4:5], s[4:5], 2
	v_ashrrev_i32_e32 v91, 31, v90
	s_add_u32 s4, s7, s4
	v_lshlrev_b64 v[2:3], 14, v[90:91]
	v_or_b32_e32 v4, 8, v90
	v_or_b32_e32 v10, 16, v90
	v_or_b32_e32 v12, 24, v90
	v_or_b32_e32 v18, 32, v90
	v_or_b32_e32 v20, 40, v90
	v_or_b32_e32 v26, 48, v90
	v_or_b32_e32 v28, 56, v90
	v_or_b32_e32 v34, 64, v90
	v_or_b32_e32 v36, 0x48, v90
	v_or_b32_e32 v42, 0x50, v90
	v_or_b32_e32 v44, 0x58, v90
	v_or_b32_e32 v66, 0x60, v90
	v_or_b32_e32 v68, 0x68, v90
	v_or_b32_e32 v94, 0x70, v90
	v_or_b32_e32 v90, 0x78, v90
	s_addc_u32 s5, s8, s5
	v_ashrrev_i32_e32 v5, 31, v4
	v_ashrrev_i32_e32 v11, 31, v10
	v_ashrrev_i32_e32 v13, 31, v12
	v_ashrrev_i32_e32 v19, 31, v18
	v_ashrrev_i32_e32 v21, 31, v20
	v_ashrrev_i32_e32 v27, 31, v26
	v_ashrrev_i32_e32 v29, 31, v28
	v_ashrrev_i32_e32 v35, 31, v34
	v_ashrrev_i32_e32 v37, 31, v36
	v_ashrrev_i32_e32 v43, 31, v42
	v_ashrrev_i32_e32 v45, 31, v44
	v_ashrrev_i32_e32 v67, 31, v66
	v_ashrrev_i32_e32 v69, 31, v68
	v_ashrrev_i32_e32 v95, 31, v94
	v_ashrrev_i32_e32 v91, 31, v90
	v_lshl_add_u64 v[92:93], s[4:5], 0, v[130:131]
	v_lshlrev_b64 v[4:5], 14, v[4:5]
	v_lshlrev_b64 v[10:11], 14, v[10:11]
	v_lshlrev_b64 v[12:13], 14, v[12:13]
	v_lshlrev_b64 v[18:19], 14, v[18:19]
	v_lshlrev_b64 v[20:21], 14, v[20:21]
	v_lshlrev_b64 v[26:27], 14, v[26:27]
	v_lshlrev_b64 v[28:29], 14, v[28:29]
	v_lshlrev_b64 v[34:35], 14, v[34:35]
	v_lshlrev_b64 v[36:37], 14, v[36:37]
	v_lshlrev_b64 v[42:43], 14, v[42:43]
	v_lshlrev_b64 v[44:45], 14, v[44:45]
	v_lshlrev_b64 v[66:67], 14, v[66:67]
	v_lshlrev_b64 v[68:69], 14, v[68:69]
	v_lshlrev_b64 v[94:95], 14, v[94:95]
	v_lshlrev_b64 v[90:91], 14, v[90:91]
	v_lshl_add_u64 v[2:3], v[92:93], 0, v[2:3]
	v_lshl_add_u64 v[6:7], v[92:93], 0, v[4:5]
	v_lshl_add_u64 v[10:11], v[92:93], 0, v[10:11]
	v_lshl_add_u64 v[14:15], v[92:93], 0, v[12:13]
	v_lshl_add_u64 v[18:19], v[92:93], 0, v[18:19]
	v_lshl_add_u64 v[22:23], v[92:93], 0, v[20:21]
	v_lshl_add_u64 v[26:27], v[92:93], 0, v[26:27]
	v_lshl_add_u64 v[30:31], v[92:93], 0, v[28:29]
	v_lshl_add_u64 v[34:35], v[92:93], 0, v[34:35]
	v_lshl_add_u64 v[38:39], v[92:93], 0, v[36:37]
	v_lshl_add_u64 v[42:43], v[92:93], 0, v[42:43]
	v_lshl_add_u64 v[46:47], v[92:93], 0, v[44:45]
	v_lshl_add_u64 v[66:67], v[92:93], 0, v[66:67]
	v_lshl_add_u64 v[70:71], v[92:93], 0, v[68:69]
	v_lshl_add_u64 v[94:95], v[92:93], 0, v[94:95]
	v_lshl_add_u64 v[96:97], v[92:93], 0, v[90:91]
	global_load_dwordx4 v[2:5], v[2:3], off nt
	s_nop 0
	global_load_dwordx4 v[6:9], v[6:7], off nt
	s_nop 0
	global_load_dwordx4 v[10:13], v[10:11], off nt
	s_nop 0
	global_load_dwordx4 v[14:17], v[14:15], off nt
	s_nop 0
	global_load_dwordx4 v[18:21], v[18:19], off nt
	s_nop 0
	global_load_dwordx4 v[22:25], v[22:23], off nt
	s_nop 0
	global_load_dwordx4 v[26:29], v[26:27], off nt
	s_nop 0
	global_load_dwordx4 v[30:33], v[30:31], off nt
	s_nop 0
	global_load_dwordx4 v[34:37], v[34:35], off nt
	s_nop 0
	global_load_dwordx4 v[38:41], v[38:39], off nt
	s_nop 0
	global_load_dwordx4 v[42:45], v[42:43], off nt
	s_nop 0
	global_load_dwordx4 v[46:49], v[46:47], off nt
	s_nop 0
	global_load_dwordx4 v[66:69], v[66:67], off nt
	s_nop 0
	global_load_dwordx4 v[70:73], v[70:71], off nt
	s_nop 0
	global_load_dwordx4 v[90:93], v[94:95], off nt
	s_nop 0
	global_load_dwordx4 v[94:97], v[96:97], off nt
	s_branch .LBB0_73
; #define MOE_RANGE(first_, end_, stride_) do { f32x4 rgA_[16], rgB_[16]; int ia_ = (first_); if (ia_ < (end_)) MOE_LOAD(ia_, rgA_); \
;         while (ia_ < (end_)) { const int ib_ = ia_ + (stride_); if (ib_ < (end_)) MOE_LOAD(ib_, rgB_); MOE_FIN(ia_, rgA_); if (ib_ >= (end_)) break; \
;             ia_ = ib_ + (stride_); if (ia_ < (end_)) MOE_LOAD(ia_, rgA_); MOE_FIN(ib_, rgB_); } } while (0)
; __global__ void __launch_bounds__(NTHREADS, 2) fwd(Args args) {
;     ...
;             if (bid >= 192) MOE_RANGE(CV_P0 + CV2 + CV2X + CV3 + CV4 - CV4P0 + (bid - 192) * NWAVES + wave, CV_P0 + CV2 + CV2X + CV3 + CV4, (G - 192) * NWAVES);
.LBB0_81:
	s_cmpk_lt_i32 s94, 0xc0
	s_branch .LBB0_93
	s_add_i32 s2, s50, 0xe400
	s_cmp_gt_i32 s2, 0xf9ff
	s_cbranch_scc1 .LBB0_84
	s_ashr_i32 s0, s2, 31
	s_lshr_b32 s0, s0, 21
	s_add_i32 s1, s2, s0
	s_ashr_i32 s0, s1, 11
	s_and_b32 s1, s1, 0xf800
	s_sub_i32 s3, s2, s1
	s_ashr_i32 s1, s0, 31
	s_lshl_b64 s[0:1], s[0:1], 25
	s_add_u32 s4, s66, s0
	s_sext_i32_i16 s0, s3
	s_addc_u32 s5, s67, s1
	s_bfe_u32 s0, s0, 0x70018
	s_add_i32 s0, s3, s0
	s_sext_i32_i16 s1, s0
	s_and_b32 s0, s0, 0xff80
	s_sub_i32 s0, s3, s0
	s_sext_i32_i16 s0, s0
	s_and_b32 s1, s1, 0xffffff80
	s_lshl_b32 s0, s0, 5
	s_waitcnt vmcnt(4)
	v_or_b32_e32 v46, s1, v1
	s_ashr_i32 s1, s0, 31
	s_lshl_b64 s[0:1], s[0:1], 2
	s_add_u32 s0, s4, s0
	v_or_b32_e32 v4, 8, v46
	v_or_b32_e32 v10, 16, v46
	v_or_b32_e32 v12, 24, v46
	v_or_b32_e32 v18, 32, v46
	v_or_b32_e32 v20, 40, v46
	v_or_b32_e32 v26, 48, v46
	v_or_b32_e32 v28, 56, v46
	v_or_b32_e32 v34, 64, v46
	v_or_b32_e32 v36, 0x48, v46
	v_or_b32_e32 v42, 0x50, v46
	v_or_b32_e32 v44, 0x58, v46
	s_addc_u32 s1, s5, s1
	v_mov_b32_e32 v131, 0
	v_ashrrev_i32_e32 v47, 31, v46
	v_ashrrev_i32_e32 v5, 31, v4
	v_ashrrev_i32_e32 v11, 31, v10
	v_ashrrev_i32_e32 v13, 31, v12
	v_ashrrev_i32_e32 v19, 31, v18
	v_ashrrev_i32_e32 v21, 31, v20
	v_ashrrev_i32_e32 v27, 31, v26
	v_ashrrev_i32_e32 v29, 31, v28
	v_ashrrev_i32_e32 v35, 31, v34
	v_ashrrev_i32_e32 v37, 31, v36
	v_ashrrev_i32_e32 v43, 31, v42
	v_ashrrev_i32_e32 v45, 31, v44
	v_lshl_add_u64 v[48:49], s[0:1], 0, v[130:131]
	v_lshlrev_b64 v[2:3], 14, v[46:47]
	v_lshlrev_b64 v[4:5], 14, v[4:5]
	v_lshlrev_b64 v[10:11], 14, v[10:11]
	v_lshlrev_b64 v[12:13], 14, v[12:13]
	v_lshlrev_b64 v[18:19], 14, v[18:19]
	v_lshlrev_b64 v[20:21], 14, v[20:21]
	v_lshlrev_b64 v[26:27], 14, v[26:27]
	v_lshlrev_b64 v[28:29], 14, v[28:29]
	v_lshlrev_b64 v[34:35], 14, v[34:35]
	v_lshlrev_b64 v[36:37], 14, v[36:37]
	v_lshlrev_b64 v[42:43], 14, v[42:43]
	v_lshlrev_b64 v[44:45], 14, v[44:45]
	v_lshl_add_u64 v[2:3], v[48:49], 0, v[2:3]
	v_lshl_add_u64 v[6:7], v[48:49], 0, v[4:5]
	v_lshl_add_u64 v[10:11], v[48:49], 0, v[10:11]
	v_lshl_add_u64 v[14:15], v[48:49], 0, v[12:13]
	v_lshl_add_u64 v[18:19], v[48:49], 0, v[18:19]
	v_lshl_add_u64 v[22:23], v[48:49], 0, v[20:21]
	v_lshl_add_u64 v[26:27], v[48:49], 0, v[26:27]
	v_lshl_add_u64 v[30:31], v[48:49], 0, v[28:29]
	v_lshl_add_u64 v[34:35], v[48:49], 0, v[34:35]
	v_lshl_add_u64 v[38:39], v[48:49], 0, v[36:37]
	v_lshl_add_u64 v[42:43], v[48:49], 0, v[42:43]
	v_lshl_add_u64 v[50:51], v[48:49], 0, v[44:45]
	global_load_dwordx4 v[2:5], v[2:3], off nt
	s_nop 0
	global_load_dwordx4 v[6:9], v[6:7], off nt
	s_nop 0
	global_load_dwordx4 v[10:13], v[10:11], off nt
	s_nop 0
	global_load_dwordx4 v[14:17], v[14:15], off nt
	s_nop 0
	global_load_dwordx4 v[18:21], v[18:19], off nt
	s_nop 0
	global_load_dwordx4 v[22:25], v[22:23], off nt
	s_nop 0
	global_load_dwordx4 v[26:29], v[26:27], off nt
	s_nop 0
	global_load_dwordx4 v[30:33], v[30:31], off nt
	s_nop 0
	global_load_dwordx4 v[34:37], v[34:35], off nt
	s_nop 0
	global_load_dwordx4 v[38:41], v[38:39], off nt
	s_nop 0
	global_load_dwordx4 v[42:45], v[42:43], off nt
	s_nop 0
	global_load_dwordx4 v[54:57], v[50:51], off nt
	v_or_b32_e32 v50, 0x60, v46
	v_ashrrev_i32_e32 v51, 31, v50
	v_or_b32_e32 v52, 0x68, v46
	v_lshlrev_b64 v[50:51], 14, v[50:51]
	v_ashrrev_i32_e32 v53, 31, v52
	v_lshl_add_u64 v[50:51], v[48:49], 0, v[50:51]
	v_lshlrev_b64 v[52:53], 14, v[52:53]
	v_lshl_add_u64 v[52:53], v[48:49], 0, v[52:53]
	global_load_dwordx4 v[66:69], v[50:51], off nt
	global_load_dwordx4 v[74:77], v[52:53], off nt
	v_or_b32_e32 v50, 0x70, v46
	v_ashrrev_i32_e32 v51, 31, v50
	v_or_b32_e32 v46, 0x78, v46
	v_lshlrev_b64 v[50:51], 14, v[50:51]
	v_ashrrev_i32_e32 v47, 31, v46
	v_lshl_add_u64 v[50:51], v[48:49], 0, v[50:51]
	v_lshlrev_b64 v[46:47], 14, v[46:47]
	v_lshl_add_u64 v[46:47], v[48:49], 0, v[46:47]
	global_load_dwordx4 v[90:93], v[50:51], off nt
	global_load_dwordx4 v[94:97], v[46:47], off nt

; #define MOE_RANGE(first_, end_, stride_) do { f32x4 rgA_[16], rgB_[16]; int ia_ = (first_); if (ia_ < (end_)) MOE_LOAD(ia_, rgA_); \
;         while (ia_ < (end_)) { const int ib_ = ia_ + (stride_); if (ib_ < (end_)) MOE_LOAD(ib_, rgB_); MOE_FIN(ia_, rgA_); if (ib_ >= (end_)) break; \
;             ia_ = ib_ + (stride_); if (ia_ < (end_)) MOE_LOAD(ia_, rgA_); MOE_FIN(ib_, rgB_); } } while (0)
; __global__ void __launch_bounds__(NTHREADS, 2) fwd(Args args) {
;     ...
;             if (bid >= 64 + NCMB && wave < 6) MOE_RANGE(CV_P0 + CV2 + CV2X + CV3 + (bid - 64 - NCMB) * 6 + wave, CV_P0 + CV2 + CV2X + CV3 + CV4 - CV4P0, (G - 64 - NCMB) * 6);
.LBB0_464:
	v_writelane_b32 v247, s22, 0
	v_writelane_b32 v247, s23, 1
	v_writelane_b32 v247, s24, 2
	v_writelane_b32 v247, s25, 3
	v_writelane_b32 v247, s26, 4
	v_writelane_b32 v247, s27, 5
	v_writelane_b32 v247, s28, 6
	v_writelane_b32 v247, s29, 7
	v_writelane_b32 v247, s30, 8
	v_writelane_b32 v247, s31, 9
	v_writelane_b32 v247, s32, 10
	v_writelane_b32 v247, s33, 11
	s_mov_b64 exec, -1
	s_waitcnt vmcnt(0)
	v_readlane_b32 s3, v246, 21
	s_nop 3
	s_cmpk_gt_i32 s94, 0xbf
	s_cbranch_scc1 .Lfc4_conv
	s_sub_i32 s2, s94, 64
	s_lshl_b32 s2, s2, 3
	s_add_i32 s2, s2, s3
	s_add_i32 s2, s2, 17408
	s_mov_b32 s4, 27328
	s_movk_i32 s33, 1024
	s_branch .Lfc4_go
.Lfc4_conv:
	s_sub_i32 s2, s94, 192
	s_lshl_b32 s2, s2, 3
	s_add_i32 s2, s2, s3
	s_mov_b32 s4, 17408
	s_movk_i32 s33, 512
.Lfc4_go:
	s_cmp_lt_u32 s2, s4
	s_cbranch_scc0 .Lfc4_done
	v_mbcnt_lo_u32_b32 v208, -1, 0
	v_mbcnt_hi_u32_b32 v208, -1, v208
	v_lshrrev_b32_e32 v204, 3, v208
	v_and_b32_e32 v208, 7, v208
	v_lshlrev_b32_e32 v205, 4, v208
	v_lshlrev_b32_e32 v206, 13, v208
	v_lshl_add_u32 v206, v204, 4, v206
	v_readlane_b32 s14, v246, 8
	v_readlane_b32 s15, v246, 9
	s_nop 3
	s_sub_u32 s14, s14, 0x100
	s_subb_u32 s15, s15, 0
	s_load_dwordx2 s[18:19], s[14:15], 0xb8
	s_load_dwordx2 s[20:21], s[14:15], 0xc8
	s_mov_b32 s22, 0x43800000
	s_mov_b32 s23, 0x43800000
	s_mov_b32 s5, 0
	s_mov_b32 s3, s2
	s_waitcnt vmcnt(0) lgkmcnt(0)
	s_mov_b32 s26, 39424
	s_cmp_ge_u32 s2, 20480
	s_cselect_b32 s26, -20480, s26
	s_cmp_ge_u32 s2, 23232
	s_cselect_b32 s26, 36672, s26
	s_add_u32 s29, s2, s26
	s_cmp_lt_u32 s29, 0x10000
	s_cbranch_scc0 .Lfc4_sdp0
	s_lshr_b32 s30, s29, 11
	s_and_b32 s26, s29, 0x7ff
	s_lshr_b32 s31, s26, 7
	s_and_b32 s32, s26, 0x7f
	s_lshl_b32 s26, s30, 25
	s_lshl_b32 s27, s31, 21
	s_add_u32 s26, s26, s27
	s_lshl_b32 s27, s32, 7
	s_add_u32 s26, s26, s27
	s_add_u32 s6, s18, s26
	s_addc_u32 s7, s19, 0
	s_movk_i32 s24, 0x4000
	s_branch .Lfc4_scp0

; __device__ __forceinline__ void item8_load(const float* W, int N, int k0, int n0, int lane, f32x4 (&rg)[16]) {
; #pragma unroll
;     for (int i = 0; i < 16; ++i) rg[i] = __builtin_nontemporal_load((const f32x4*)(W + (size_t)(k0 + 8 * i + (lane >> 3)) * N + n0 + 4 * (lane & 7)));
; }
.Lfc4_scp0:
	s_lshl_b32 s25, s24, 4
	v_mad_u32_u24 v207, v204, s25, v205
	global_load_dwordx4 v[2:5], v207, s[6:7] nt
	s_add_u32 s6, s6, s24
	s_addc_u32 s7, s7, 0
	global_load_dwordx4 v[6:9], v207, s[6:7] nt
	s_add_u32 s6, s6, s24
	s_addc_u32 s7, s7, 0
	global_load_dwordx4 v[10:13], v207, s[6:7] nt
	s_add_u32 s6, s6, s24
	s_addc_u32 s7, s7, 0
	global_load_dwordx4 v[14:17], v207, s[6:7] nt
	s_add_u32 s6, s6, s24
	s_addc_u32 s7, s7, 0
	global_load_dwordx4 v[18:21], v207, s[6:7] nt
	s_add_u32 s6, s6, s24
	s_addc_u32 s7, s7, 0
	global_load_dwordx4 v[22:25], v207, s[6:7] nt
	s_add_u32 s6, s6, s24
	s_addc_u32 s7, s7, 0
	global_load_dwordx4 v[26:29], v207, s[6:7] nt
	s_add_u32 s6, s6, s24
	s_addc_u32 s7, s7, 0
	global_load_dwordx4 v[30:33], v207, s[6:7] nt
	s_add_u32 s6, s6, s24
	s_addc_u32 s7, s7, 0
	global_load_dwordx4 v[34:37], v207, s[6:7] nt
	s_add_u32 s6, s6, s24
	s_addc_u32 s7, s7, 0
	global_load_dwordx4 v[38:41], v207, s[6:7] nt
	s_add_u32 s6, s6, s24
	s_addc_u32 s7, s7, 0
	global_load_dwordx4 v[42:45], v207, s[6:7] nt
	s_add_u32 s6, s6, s24
	s_addc_u32 s7, s7, 0
	global_load_dwordx4 v[46:49], v207, s[6:7] nt
	s_add_u32 s6, s6, s24
	s_addc_u32 s7, s7, 0
	global_load_dwordx4 v[50:53], v207, s[6:7] nt
	s_add_u32 s6, s6, s24
	s_addc_u32 s7, s7, 0
	global_load_dwordx4 v[54:57], v207, s[6:7] nt
	s_add_u32 s6, s6, s24
	s_addc_u32 s7, s7, 0
	global_load_dwordx4 v[58:61], v207, s[6:7] nt
	s_add_u32 s6, s6, s24
	s_addc_u32 s7, s7, 0
	global_load_dwordx4 v[62:65], v207, s[6:7] nt
	s_add_u32 s2, s2, s33
	s_cmp_lt_u32 s2, s4
	s_cbranch_scc0 .Lfc4_body0
	s_mov_b32 s26, 39424
	s_cmp_ge_u32 s2, 20480
	s_cselect_b32 s26, -20480, s26
	s_cmp_ge_u32 s2, 23232
	s_cselect_b32 s26, 36672, s26
	s_add_u32 s29, s2, s26
	s_cmp_lt_u32 s29, 0x10000
	s_cbranch_scc0 .Lfc4_sdp1
	s_lshr_b32 s30, s29, 11
	s_and_b32 s26, s29, 0x7ff
	s_lshr_b32 s31, s26, 7
	s_and_b32 s32, s26, 0x7f
	s_lshl_b32 s26, s30, 25
	s_lshl_b32 s27, s31, 21
	s_add_u32 s26, s26, s27
	s_lshl_b32 s27, s32, 7
	s_add_u32 s26, s26, s27
	s_add_u32 s6, s18, s26
	s_addc_u32 s7, s19, 0
	s_movk_i32 s24, 0x4000
	s_branch .Lfc4_scp1

.Lfc4_body0:
	s_add_u32 s2, s2, s33
	s_cmp_lt_u32 s2, s4
	s_cbranch_scc0 .Lfc4_nl0
	s_mov_b32 s26, 39424
	s_cmp_ge_u32 s2, 20480
	s_cselect_b32 s26, -20480, s26
	s_cmp_ge_u32 s2, 23232
	s_cselect_b32 s26, 36672, s26
	s_add_u32 s29, s2, s26
	s_cmp_lt_u32 s29, 0x10000
	s_cbranch_scc0 .Lfc4_sdb0
	s_lshr_b32 s30, s29, 11
	s_and_b32 s26, s29, 0x7ff
	s_lshr_b32 s31, s26, 7
	s_and_b32 s32, s26, 0x7f
	s_lshl_b32 s26, s30, 25
	s_lshl_b32 s27, s31, 21
	s_add_u32 s26, s26, s27
	s_lshl_b32 s27, s32, 7
	s_add_u32 s26, s26, s27
	s_add_u32 s6, s18, s26
	s_addc_u32 s7, s19, 0
	s_movk_i32 s24, 0x4000
	s_branch .Lfc4_scb0

; __device__ __forceinline__ void item8_load(const float* W, int N, int k0, int n0, int lane, f32x4 (&rg)[16]) {
; #pragma unroll
;     for (int i = 0; i < 16; ++i) rg[i] = __builtin_nontemporal_load((const f32x4*)(W + (size_t)(k0 + 8 * i + (lane >> 3)) * N + n0 + 4 * (lane & 7)));
; }
.Lfc4_scb0:
	s_lshl_b32 s25, s24, 4
	v_mad_u32_u24 v207, v204, s25, v205
	global_load_dwordx4 v[130:133], v207, s[6:7] nt
	s_add_u32 s6, s6, s24
	s_addc_u32 s7, s7, 0
	global_load_dwordx4 v[134:137], v207, s[6:7] nt
	s_add_u32 s6, s6, s24
	s_addc_u32 s7, s7, 0
	global_load_dwordx4 v[138:141], v207, s[6:7] nt
	s_add_u32 s6, s6, s24
	s_addc_u32 s7, s7, 0
	global_load_dwordx4 v[142:145], v207, s[6:7] nt
	s_add_u32 s6, s6, s24
	s_addc_u32 s7, s7, 0
	global_load_dwordx4 v[146:149], v207, s[6:7] nt
	s_add_u32 s6, s6, s24
	s_addc_u32 s7, s7, 0
	global_load_dwordx4 v[150:153], v207, s[6:7] nt
	s_add_u32 s6, s6, s24
	s_addc_u32 s7, s7, 0
	global_load_dwordx4 v[154:157], v207, s[6:7] nt
	s_add_u32 s6, s6, s24
	s_addc_u32 s7, s7, 0
	global_load_dwordx4 v[158:161], v207, s[6:7] nt
	s_add_u32 s6, s6, s24
	s_addc_u32 s7, s7, 0
	global_load_dwordx4 v[162:165], v207, s[6:7] nt
	s_add_u32 s6, s6, s24
	s_addc_u32 s7, s7, 0
	global_load_dwordx4 v[166:169], v207, s[6:7] nt
	s_add_u32 s6, s6, s24
	s_addc_u32 s7, s7, 0
	global_load_dwordx4 v[170:173], v207, s[6:7] nt
	s_add_u32 s6, s6, s24
	s_addc_u32 s7, s7, 0
	global_load_dwordx4 v[174:177], v207, s[6:7] nt
	s_add_u32 s6, s6, s24
	s_addc_u32 s7, s7, 0
	global_load_dwordx4 v[178:181], v207, s[6:7] nt
	s_add_u32 s6, s6, s24
	s_addc_u32 s7, s7, 0
	global_load_dwordx4 v[182:185], v207, s[6:7] nt
	s_add_u32 s6, s6, s24
	s_addc_u32 s7, s7, 0
	global_load_dwordx4 v[186:189], v207, s[6:7] nt
	s_add_u32 s6, s6, s24
	s_addc_u32 s7, s7, 0
	global_load_dwordx4 v[190:193], v207, s[6:7] nt
	s_mov_b32 s26, 39424
	s_cmp_ge_u32 s3, 20480
	s_cselect_b32 s26, -20480, s26
	s_cmp_ge_u32 s3, 23232
	s_cselect_b32 s26, 36672, s26
	s_add_u32 s29, s3, s26
	s_cmp_lt_u32 s29, 0x10000
	s_cbranch_scc0 .Lfc4_ddb0
	s_lshr_b32 s30, s29, 11
	s_and_b32 s26, s29, 0x7ff
	s_lshr_b32 s31, s26, 7
	s_and_b32 s32, s26, 0x7f
	s_and_b32 s26, s32, 63
	s_lshr_b32 s26, s26, 2
	s_lshl_b32 s26, s26, 8
	s_lshr_b32 s27, s32, 6
	s_lshl_b32 s27, s27, 7
	s_add_u32 s26, s26, s27
	s_and_b32 s27, s32, 3
	s_lshl_b32 s27, s27, 5
	s_add_u32 s26, s26, s27
	s_lshl_b32 s26, s26, 11
	s_lshl_b32 s27, s30, 23
	s_add_u32 s26, s26, s27
	s_lshl_b32 s27, s31, 7
	s_add_u32 s26, s26, s27
	s_add_u32 s26, s26, 0x4001000
	s_branch .Lfc4_dcb0

.Lfc4_nl0:
	s_mov_b32 s26, 39424
	s_cmp_ge_u32 s3, 20480
	s_cselect_b32 s26, -20480, s26
	s_cmp_ge_u32 s3, 23232
	s_cselect_b32 s26, 36672, s26
	s_add_u32 s29, s3, s26
	s_cmp_lt_u32 s29, 0x10000
	s_cbranch_scc0 .Lfc4_ddn0
	s_lshr_b32 s30, s29, 11
	s_and_b32 s26, s29, 0x7ff
	s_lshr_b32 s31, s26, 7
	s_and_b32 s32, s26, 0x7f
	s_and_b32 s26, s32, 63
	s_lshr_b32 s26, s26, 2
	s_lshl_b32 s26, s26, 8
	s_lshr_b32 s27, s32, 6
	s_lshl_b32 s27, s27, 7
	s_add_u32 s26, s26, s27
	s_and_b32 s27, s32, 3
	s_lshl_b32 s27, s27, 5
	s_add_u32 s26, s26, s27
	s_lshl_b32 s26, s26, 11
	s_lshl_b32 s27, s30, 23
	s_add_u32 s26, s26, s27
	s_lshl_b32 s27, s31, 7
	s_add_u32 s26, s26, s27
	s_add_u32 s26, s26, 0x4001000
	s_branch .Lfc4_dcn0

; __device__ __forceinline__ void item8_load(const float* W, int N, int k0, int n0, int lane, f32x4 (&rg)[16]) {
; #pragma unroll
;     for (int i = 0; i < 16; ++i) rg[i] = __builtin_nontemporal_load((const f32x4*)(W + (size_t)(k0 + 8 * i + (lane >> 3)) * N + n0 + 4 * (lane & 7)));
; }
.Lfc4_scb1:
	s_lshl_b32 s25, s24, 4
	v_mad_u32_u24 v207, v204, s25, v205
	global_load_dwordx4 v[2:5], v207, s[6:7] nt
	s_add_u32 s6, s6, s24
	s_addc_u32 s7, s7, 0
	global_load_dwordx4 v[6:9], v207, s[6:7] nt
	s_add_u32 s6, s6, s24
	s_addc_u32 s7, s7, 0
	global_load_dwordx4 v[10:13], v207, s[6:7] nt
	s_add_u32 s6, s6, s24
	s_addc_u32 s7, s7, 0
	global_load_dwordx4 v[14:17], v207, s[6:7] nt
	s_add_u32 s6, s6, s24
	s_addc_u32 s7, s7, 0
	global_load_dwordx4 v[18:21], v207, s[6:7] nt
	s_add_u32 s6, s6, s24
	s_addc_u32 s7, s7, 0
	global_load_dwordx4 v[22:25], v207, s[6:7] nt
	s_add_u32 s6, s6, s24
	s_addc_u32 s7, s7, 0
	global_load_dwordx4 v[26:29], v207, s[6:7] nt
	s_add_u32 s6, s6, s24
	s_addc_u32 s7, s7, 0
	global_load_dwordx4 v[30:33], v207, s[6:7] nt
	s_add_u32 s6, s6, s24
	s_addc_u32 s7, s7, 0
	global_load_dwordx4 v[34:37], v207, s[6:7] nt
	s_add_u32 s6, s6, s24
	s_addc_u32 s7, s7, 0
	global_load_dwordx4 v[38:41], v207, s[6:7] nt
	s_add_u32 s6, s6, s24
	s_addc_u32 s7, s7, 0
	global_load_dwordx4 v[42:45], v207, s[6:7] nt
	s_add_u32 s6, s6, s24
	s_addc_u32 s7, s7, 0
	global_load_dwordx4 v[46:49], v207, s[6:7] nt
	s_add_u32 s6, s6, s24
	s_addc_u32 s7, s7, 0
	global_load_dwordx4 v[50:53], v207, s[6:7] nt
	s_add_u32 s6, s6, s24
	s_addc_u32 s7, s7, 0
	global_load_dwordx4 v[54:57], v207, s[6:7] nt
	s_add_u32 s6, s6, s24
	s_addc_u32 s7, s7, 0
	global_load_dwordx4 v[58:61], v207, s[6:7] nt
	s_add_u32 s6, s6, s24
	s_addc_u32 s7, s7, 0
	global_load_dwordx4 v[62:65], v207, s[6:7] nt
	s_mov_b32 s26, 39424
	s_cmp_ge_u32 s3, 20480
	s_cselect_b32 s26, -20480, s26
	s_cmp_ge_u32 s3, 23232
	s_cselect_b32 s26, 36672, s26
	s_add_u32 s29, s3, s26
	s_cmp_lt_u32 s29, 0x10000
	s_cbranch_scc0 .Lfc4_ddb1
	s_lshr_b32 s30, s29, 11
	s_and_b32 s26, s29, 0x7ff
	s_lshr_b32 s31, s26, 7
	s_and_b32 s32, s26, 0x7f
	s_and_b32 s26, s32, 63
	s_lshr_b32 s26, s26, 2
	s_lshl_b32 s26, s26, 8
	s_lshr_b32 s27, s32, 6
	s_lshl_b32 s27, s27, 7
	s_add_u32 s26, s26, s27
	s_and_b32 s27, s32, 3
	s_lshl_b32 s27, s27, 5
	s_add_u32 s26, s26, s27
	s_lshl_b32 s26, s26, 11
	s_lshl_b32 s27, s30, 23
	s_add_u32 s26, s26, s27
	s_lshl_b32 s27, s31, 7
	s_add_u32 s26, s26, s27
	s_add_u32 s26, s26, 0x4001000
	s_branch .Lfc4_dcb1

; __device__ __forceinline__ void item8_load(const float* W, int N, int k0, int n0, int lane, f32x4 (&rg)[16]) {
; #pragma unroll
;     for (int i = 0; i < 16; ++i) rg[i] = __builtin_nontemporal_load((const f32x4*)(W + (size_t)(k0 + 8 * i + (lane >> 3)) * N + n0 + 4 * (lane & 7)));
; }
.Lfc4_scb2:
	s_lshl_b32 s25, s24, 4
	v_mad_u32_u24 v207, v204, s25, v205
	global_load_dwordx4 v[66:69], v207, s[6:7] nt
	s_add_u32 s6, s6, s24
	s_addc_u32 s7, s7, 0
	global_load_dwordx4 v[70:73], v207, s[6:7] nt
	s_add_u32 s6, s6, s24
	s_addc_u32 s7, s7, 0
	global_load_dwordx4 v[74:77], v207, s[6:7] nt
	s_add_u32 s6, s6, s24
	s_addc_u32 s7, s7, 0
	global_load_dwordx4 v[78:81], v207, s[6:7] nt
	s_add_u32 s6, s6, s24
	s_addc_u32 s7, s7, 0
	global_load_dwordx4 v[82:85], v207, s[6:7] nt
	s_add_u32 s6, s6, s24
	s_addc_u32 s7, s7, 0
	global_load_dwordx4 v[86:89], v207, s[6:7] nt
	s_add_u32 s6, s6, s24
	s_addc_u32 s7, s7, 0
	global_load_dwordx4 v[90:93], v207, s[6:7] nt
	s_add_u32 s6, s6, s24
	s_addc_u32 s7, s7, 0
	global_load_dwordx4 v[94:97], v207, s[6:7] nt
	s_add_u32 s6, s6, s24
	s_addc_u32 s7, s7, 0
	global_load_dwordx4 v[98:101], v207, s[6:7] nt
	s_add_u32 s6, s6, s24
	s_addc_u32 s7, s7, 0
	global_load_dwordx4 v[102:105], v207, s[6:7] nt
	s_add_u32 s6, s6, s24
	s_addc_u32 s7, s7, 0
	global_load_dwordx4 v[106:109], v207, s[6:7] nt
	s_add_u32 s6, s6, s24
	s_addc_u32 s7, s7, 0
	global_load_dwordx4 v[110:113], v207, s[6:7] nt
	s_add_u32 s6, s6, s24
	s_addc_u32 s7, s7, 0
	global_load_dwordx4 v[114:117], v207, s[6:7] nt
	s_add_u32 s6, s6, s24
	s_addc_u32 s7, s7, 0
	global_load_dwordx4 v[118:121], v207, s[6:7] nt
	s_add_u32 s6, s6, s24
	s_addc_u32 s7, s7, 0
	global_load_dwordx4 v[122:125], v207, s[6:7] nt
	s_add_u32 s6, s6, s24
	s_addc_u32 s7, s7, 0
	global_load_dwordx4 v[126:129], v207, s[6:7] nt
	s_mov_b32 s26, 39424
	s_cmp_ge_u32 s3, 20480
	s_cselect_b32 s26, -20480, s26
	s_cmp_ge_u32 s3, 23232
	s_cselect_b32 s26, 36672, s26
	s_add_u32 s29, s3, s26
	s_cmp_lt_u32 s29, 0x10000
	s_cbranch_scc0 .Lfc4_ddb2
	s_lshr_b32 s30, s29, 11
	s_and_b32 s26, s29, 0x7ff
	s_lshr_b32 s31, s26, 7
	s_and_b32 s32, s26, 0x7f
	s_and_b32 s26, s32, 63
	s_lshr_b32 s26, s26, 2
	s_lshl_b32 s26, s26, 8
	s_lshr_b32 s27, s32, 6
	s_lshl_b32 s27, s27, 7
	s_add_u32 s26, s26, s27
	s_and_b32 s27, s32, 3
	s_lshl_b32 s27, s27, 5
	s_add_u32 s26, s26, s27
	s_lshl_b32 s26, s26, 11
	s_lshl_b32 s27, s30, 23
	s_add_u32 s26, s26, s27
	s_lshl_b32 s27, s31, 7
	s_add_u32 s26, s26, s27
	s_add_u32 s26, s26, 0x4001000
	s_branch .Lfc4_dcb2
